# v99 + nt on the attention phase's O stores
# baseline (speedup 1.0000x reference)
.LBB0_1120:
	s_and_saveexec_b64 s[2:3], s[4:5]
	ds_write_b32 v167, v174
	s_or_b64 exec, exec, s[2:3]
	s_waitcnt lgkmcnt(0)
	ds_read_b32 v3, v161
	v_and_b32_e32 v2, 64, v159
	v_xor_b32_e32 v0, 1, v159
	v_add_u32_e32 v2, 64, v2
	v_cmp_lt_i32_e32 vcc, v0, v2
	s_waitcnt lgkmcnt(0)
	v_rcp_f32_e32 v7, v3
	s_add_u32 s2, s86, s36
	v_cndmask_b32_e32 v0, v159, v0, vcc
	v_lshlrev_b32_e32 v6, 2, v0
	v_mul_f32_e32 v8, v64, v7
	ds_bpermute_b32 v9, v6, v8
	v_and_b32_e32 v0, 1, v146
	s_addc_u32 s3, s87, s37
	v_cmp_eq_u32_e32 vcc, 0, v0
	v_lshlrev_b32_e32 v0, 1, v145
	v_ashrrev_i32_e32 v145, 31, v144
	v_lshl_add_u64 v[2:3], s[2:3], 0, v[0:1]
	v_lshlrev_b64 v[4:5], 12, v[144:145]
	v_lshl_add_u64 v[4:5], v[2:3], 0, v[4:5]
	s_and_saveexec_b64 s[2:3], vcc
	s_cbranch_execz .LBB0_1124
	s_waitcnt lgkmcnt(0)
	v_cvt_pk_bf16_f32 v0, v8, v9
	global_store_dword v[4:5], v0, off nt
.LBB0_1124:
	s_or_b64 exec, exec, s[2:3]
	v_mul_f32_e32 v0, v48, v7
	ds_bpermute_b32 v8, v6, v0
	s_and_saveexec_b64 s[2:3], vcc
	s_cbranch_execz .LBB0_1126
	s_waitcnt lgkmcnt(0)
	v_cvt_pk_bf16_f32 v0, v0, v8
	global_store_dword v[4:5], v0, off offset:64 nt
.LBB0_1126:
	s_or_b64 exec, exec, s[2:3]
	v_mul_f32_e32 v0, v32, v7
	s_waitcnt lgkmcnt(0)
	ds_bpermute_b32 v8, v6, v0
	s_and_saveexec_b64 s[2:3], vcc
	s_cbranch_execz .LBB0_1128
	s_waitcnt lgkmcnt(0)
	v_cvt_pk_bf16_f32 v0, v0, v8
	global_store_dword v[4:5], v0, off offset:128 nt
.LBB0_1128:
	s_or_b64 exec, exec, s[2:3]
	v_mul_f32_e32 v0, v16, v7
	ds_bpermute_b32 v7, v6, v0
	s_and_saveexec_b64 s[2:3], vcc
	s_cbranch_execz .LBB0_1130
	s_waitcnt lgkmcnt(0)
	v_cvt_pk_bf16_f32 v0, v0, v7
	global_store_dword v[4:5], v0, off offset:192 nt
.LBB0_1130:
	s_or_b64 exec, exec, s[2:3]
	ds_read_b32 v0, v161 offset:4
	v_or_b32_e32 v4, 1, v144
	v_ashrrev_i32_e32 v5, 31, v4
	v_lshlrev_b64 v[4:5], 12, v[4:5]
	v_lshl_add_u64 v[4:5], v[2:3], 0, v[4:5]
	s_waitcnt lgkmcnt(0)
	v_rcp_f32_e32 v0, v0
	s_nop 0
	v_mul_f32_e32 v7, v65, v0
	ds_bpermute_b32 v8, v6, v7
	s_and_saveexec_b64 s[2:3], vcc
	s_cbranch_execz .LBB0_1132
	s_waitcnt lgkmcnt(0)
	v_cvt_pk_bf16_f32 v7, v7, v8
	global_store_dword v[4:5], v7, off nt
.LBB0_1132:
	s_or_b64 exec, exec, s[2:3]
	v_mul_f32_e32 v7, v49, v0
	s_waitcnt lgkmcnt(0)
	ds_bpermute_b32 v8, v6, v7
	s_and_saveexec_b64 s[2:3], vcc
	s_cbranch_execz .LBB0_1134
	s_waitcnt lgkmcnt(0)
	v_cvt_pk_bf16_f32 v7, v7, v8
	global_store_dword v[4:5], v7, off offset:64 nt
.LBB0_1134:
	s_or_b64 exec, exec, s[2:3]
	v_mul_f32_e32 v7, v33, v0
	s_waitcnt lgkmcnt(0)
	ds_bpermute_b32 v8, v6, v7
	s_and_saveexec_b64 s[2:3], vcc
	s_cbranch_execz .LBB0_1136
	s_waitcnt lgkmcnt(0)
	v_cvt_pk_bf16_f32 v7, v7, v8
	global_store_dword v[4:5], v7, off offset:128 nt
.LBB0_1136:
	s_or_b64 exec, exec, s[2:3]
	v_mul_f32_e32 v0, v17, v0
	ds_bpermute_b32 v7, v6, v0
	s_and_saveexec_b64 s[2:3], vcc
	s_cbranch_execz .LBB0_1138
	s_waitcnt lgkmcnt(0)
	v_cvt_pk_bf16_f32 v0, v0, v7
	global_store_dword v[4:5], v0, off offset:192 nt
.LBB0_1138:
	s_or_b64 exec, exec, s[2:3]
	ds_read_b32 v0, v161 offset:8
	v_or_b32_e32 v4, 2, v144
	v_ashrrev_i32_e32 v5, 31, v4
	v_lshlrev_b64 v[4:5], 12, v[4:5]
	v_lshl_add_u64 v[4:5], v[2:3], 0, v[4:5]
	s_waitcnt lgkmcnt(0)
	v_rcp_f32_e32 v0, v0
	s_nop 0
	v_mul_f32_e32 v7, v66, v0
	ds_bpermute_b32 v8, v6, v7
	s_and_saveexec_b64 s[2:3], vcc
	s_cbranch_execz .LBB0_1140
	s_waitcnt lgkmcnt(0)
	v_cvt_pk_bf16_f32 v7, v7, v8
	global_store_dword v[4:5], v7, off nt
.LBB0_1140:
	s_or_b64 exec, exec, s[2:3]
	v_mul_f32_e32 v7, v50, v0
	s_waitcnt lgkmcnt(0)
	ds_bpermute_b32 v8, v6, v7
	s_and_saveexec_b64 s[2:3], vcc
	s_cbranch_execz .LBB0_1142
	s_waitcnt lgkmcnt(0)
	v_cvt_pk_bf16_f32 v7, v7, v8
	global_store_dword v[4:5], v7, off offset:64 nt
.LBB0_1142:
	s_or_b64 exec, exec, s[2:3]
	v_mul_f32_e32 v7, v34, v0
	s_waitcnt lgkmcnt(0)
	ds_bpermute_b32 v8, v6, v7
	s_and_saveexec_b64 s[2:3], vcc
	s_cbranch_execz .LBB0_1144
	s_waitcnt lgkmcnt(0)
	v_cvt_pk_bf16_f32 v7, v7, v8
	global_store_dword v[4:5], v7, off offset:128 nt
.LBB0_1144:
	s_or_b64 exec, exec, s[2:3]
	v_mul_f32_e32 v0, v18, v0
	ds_bpermute_b32 v7, v6, v0
	s_and_saveexec_b64 s[2:3], vcc
	s_cbranch_execz .LBB0_1146
	s_waitcnt lgkmcnt(0)
	v_cvt_pk_bf16_f32 v0, v0, v7
	global_store_dword v[4:5], v0, off offset:192 nt
.LBB0_1146:
	s_or_b64 exec, exec, s[2:3]
	ds_read_b32 v0, v161 offset:12
	v_or_b32_e32 v4, 3, v144
	v_ashrrev_i32_e32 v5, 31, v4
	v_lshlrev_b64 v[4:5], 12, v[4:5]
	v_lshl_add_u64 v[4:5], v[2:3], 0, v[4:5]
	s_waitcnt lgkmcnt(0)
	v_rcp_f32_e32 v0, v0
	s_nop 0
	v_mul_f32_e32 v7, v67, v0
	ds_bpermute_b32 v8, v6, v7
	s_and_saveexec_b64 s[2:3], vcc
	s_cbranch_execz .LBB0_1148
	s_waitcnt lgkmcnt(0)
	v_cvt_pk_bf16_f32 v7, v7, v8
	global_store_dword v[4:5], v7, off nt
.LBB0_1148:
	s_or_b64 exec, exec, s[2:3]
	v_mul_f32_e32 v7, v51, v0
	s_waitcnt lgkmcnt(0)
	ds_bpermute_b32 v8, v6, v7
	s_and_saveexec_b64 s[2:3], vcc
	s_cbranch_execz .LBB0_1150
	s_waitcnt lgkmcnt(0)
	v_cvt_pk_bf16_f32 v7, v7, v8
	global_store_dword v[4:5], v7, off offset:64 nt
.LBB0_1150:
	s_or_b64 exec, exec, s[2:3]
	v_mul_f32_e32 v7, v35, v0
	s_waitcnt lgkmcnt(0)
	ds_bpermute_b32 v8, v6, v7
	s_and_saveexec_b64 s[2:3], vcc
	s_cbranch_execz .LBB0_1152
	s_waitcnt lgkmcnt(0)
	v_cvt_pk_bf16_f32 v7, v7, v8
	global_store_dword v[4:5], v7, off offset:128 nt
.LBB0_1152:
	s_or_b64 exec, exec, s[2:3]
	v_mul_f32_e32 v0, v19, v0
	ds_bpermute_b32 v7, v6, v0
	s_and_saveexec_b64 s[2:3], vcc
	s_cbranch_execz .LBB0_1154
	s_waitcnt lgkmcnt(0)
	v_cvt_pk_bf16_f32 v0, v0, v7
	global_store_dword v[4:5], v0, off offset:192 nt
.LBB0_1154:
	s_or_b64 exec, exec, s[2:3]
	ds_read_b32 v0, v161 offset:32
	v_lshlrev_b64 v[4:5], 12, v[144:145]
	v_lshl_add_u64 v[4:5], v[2:3], 0, v[4:5]
	s_mov_b64 s[2:3], 0x8000
	v_lshl_add_u64 v[4:5], v[4:5], 0, s[2:3]
	s_waitcnt lgkmcnt(0)
	v_rcp_f32_e32 v0, v0
	s_nop 0
	v_mul_f32_e32 v7, v68, v0
	ds_bpermute_b32 v8, v6, v7
	s_and_saveexec_b64 s[2:3], vcc
	s_cbranch_execz .LBB0_1156
	s_waitcnt lgkmcnt(0)
	v_cvt_pk_bf16_f32 v7, v7, v8
	global_store_dword v[4:5], v7, off nt
.LBB0_1156:
	s_or_b64 exec, exec, s[2:3]
	v_mul_f32_e32 v7, v52, v0
	s_waitcnt lgkmcnt(0)
	ds_bpermute_b32 v8, v6, v7
	s_and_saveexec_b64 s[2:3], vcc
	s_cbranch_execz .LBB0_1158
	s_waitcnt lgkmcnt(0)
	v_cvt_pk_bf16_f32 v7, v7, v8
	global_store_dword v[4:5], v7, off offset:64 nt
.LBB0_1158:
	s_or_b64 exec, exec, s[2:3]
	v_mul_f32_e32 v7, v36, v0
	s_waitcnt lgkmcnt(0)
	ds_bpermute_b32 v8, v6, v7
	s_and_saveexec_b64 s[2:3], vcc
	s_cbranch_execz .LBB0_1160
	s_waitcnt lgkmcnt(0)
	v_cvt_pk_bf16_f32 v7, v7, v8
	global_store_dword v[4:5], v7, off offset:128 nt
.LBB0_1160:
	s_or_b64 exec, exec, s[2:3]
	v_mul_f32_e32 v0, v20, v0
	ds_bpermute_b32 v7, v6, v0
	s_and_saveexec_b64 s[2:3], vcc
	s_cbranch_execz .LBB0_1162
	s_waitcnt lgkmcnt(0)
	v_cvt_pk_bf16_f32 v0, v0, v7
	global_store_dword v[4:5], v0, off offset:192 nt
.LBB0_1162:
	s_or_b64 exec, exec, s[2:3]
	ds_read_b32 v0, v161 offset:36
	v_lshlrev_b64 v[4:5], 12, v[144:145]
	v_lshl_add_u64 v[4:5], v[2:3], 0, v[4:5]
	s_mov_b64 s[2:3], 0x9000
	v_lshl_add_u64 v[4:5], v[4:5], 0, s[2:3]
	s_waitcnt lgkmcnt(0)
	v_rcp_f32_e32 v0, v0
	s_nop 0
	v_mul_f32_e32 v7, v69, v0
	ds_bpermute_b32 v8, v6, v7
	s_and_saveexec_b64 s[2:3], vcc
	s_cbranch_execz .LBB0_1164
	s_waitcnt lgkmcnt(0)
	v_cvt_pk_bf16_f32 v7, v7, v8
	global_store_dword v[4:5], v7, off nt
.LBB0_1164:
	s_or_b64 exec, exec, s[2:3]
	v_mul_f32_e32 v7, v53, v0
	s_waitcnt lgkmcnt(0)
	ds_bpermute_b32 v8, v6, v7
	s_and_saveexec_b64 s[2:3], vcc
	s_cbranch_execz .LBB0_1166
	s_waitcnt lgkmcnt(0)
	v_cvt_pk_bf16_f32 v7, v7, v8
	global_store_dword v[4:5], v7, off offset:64 nt
.LBB0_1166:
	s_or_b64 exec, exec, s[2:3]
	v_mul_f32_e32 v7, v37, v0
	s_waitcnt lgkmcnt(0)
	ds_bpermute_b32 v8, v6, v7
	s_and_saveexec_b64 s[2:3], vcc
	s_cbranch_execz .LBB0_1168
	s_waitcnt lgkmcnt(0)
	v_cvt_pk_bf16_f32 v7, v7, v8
	global_store_dword v[4:5], v7, off offset:128 nt
.LBB0_1168:
	s_or_b64 exec, exec, s[2:3]
	v_mul_f32_e32 v0, v21, v0
	ds_bpermute_b32 v7, v6, v0
	s_and_saveexec_b64 s[2:3], vcc
	s_cbranch_execz .LBB0_1170
	s_waitcnt lgkmcnt(0)
	v_cvt_pk_bf16_f32 v0, v0, v7
	global_store_dword v[4:5], v0, off offset:192 nt
.LBB0_1170:
	s_or_b64 exec, exec, s[2:3]
	ds_read_b32 v0, v161 offset:40
	v_lshlrev_b64 v[4:5], 12, v[144:145]
	v_lshl_add_u64 v[4:5], v[2:3], 0, v[4:5]
	s_mov_b64 s[2:3], 0xa000
	v_lshl_add_u64 v[4:5], v[4:5], 0, s[2:3]
	s_waitcnt lgkmcnt(0)
	v_rcp_f32_e32 v0, v0
	s_nop 0
	v_mul_f32_e32 v7, v70, v0
	ds_bpermute_b32 v8, v6, v7
	s_and_saveexec_b64 s[2:3], vcc
	s_cbranch_execz .LBB0_1172
	s_waitcnt lgkmcnt(0)
	v_cvt_pk_bf16_f32 v7, v7, v8
	global_store_dword v[4:5], v7, off nt
.LBB0_1172:
	s_or_b64 exec, exec, s[2:3]
	v_mul_f32_e32 v7, v54, v0
	s_waitcnt lgkmcnt(0)
	ds_bpermute_b32 v8, v6, v7
	s_and_saveexec_b64 s[2:3], vcc
	s_cbranch_execz .LBB0_1174
	s_waitcnt lgkmcnt(0)
	v_cvt_pk_bf16_f32 v7, v7, v8
	global_store_dword v[4:5], v7, off offset:64 nt
.LBB0_1174:
	s_or_b64 exec, exec, s[2:3]
	v_mul_f32_e32 v7, v38, v0
	s_waitcnt lgkmcnt(0)
	ds_bpermute_b32 v8, v6, v7
	s_and_saveexec_b64 s[2:3], vcc
	s_cbranch_execz .LBB0_1176
	s_waitcnt lgkmcnt(0)
	v_cvt_pk_bf16_f32 v7, v7, v8
	global_store_dword v[4:5], v7, off offset:128 nt
.LBB0_1176:
	s_or_b64 exec, exec, s[2:3]
	v_mul_f32_e32 v0, v22, v0
	ds_bpermute_b32 v7, v6, v0
	s_and_saveexec_b64 s[2:3], vcc
	s_cbranch_execz .LBB0_1178
	s_waitcnt lgkmcnt(0)
	v_cvt_pk_bf16_f32 v0, v0, v7
	global_store_dword v[4:5], v0, off offset:192 nt
.LBB0_1178:
	s_or_b64 exec, exec, s[2:3]
	ds_read_b32 v0, v161 offset:44
	v_lshlrev_b64 v[4:5], 12, v[144:145]
	v_lshl_add_u64 v[4:5], v[2:3], 0, v[4:5]
	s_mov_b64 s[2:3], 0xb000
	v_lshl_add_u64 v[4:5], v[4:5], 0, s[2:3]
	s_waitcnt lgkmcnt(0)
	v_rcp_f32_e32 v0, v0
	s_nop 0
	v_mul_f32_e32 v7, v71, v0
	ds_bpermute_b32 v8, v6, v7
	s_and_saveexec_b64 s[2:3], vcc
	s_cbranch_execz .LBB0_1180
	s_waitcnt lgkmcnt(0)
	v_cvt_pk_bf16_f32 v7, v7, v8
	global_store_dword v[4:5], v7, off nt
.LBB0_1180:
	s_or_b64 exec, exec, s[2:3]
	v_mul_f32_e32 v7, v55, v0
	s_waitcnt lgkmcnt(0)
	ds_bpermute_b32 v8, v6, v7
	s_and_saveexec_b64 s[2:3], vcc
	s_cbranch_execz .LBB0_1182
	s_waitcnt lgkmcnt(0)
	v_cvt_pk_bf16_f32 v7, v7, v8
	global_store_dword v[4:5], v7, off offset:64 nt
.LBB0_1182:
	s_or_b64 exec, exec, s[2:3]
	v_mul_f32_e32 v7, v39, v0
	s_waitcnt lgkmcnt(0)
	ds_bpermute_b32 v8, v6, v7
	s_and_saveexec_b64 s[2:3], vcc
	s_cbranch_execz .LBB0_1184
	s_waitcnt lgkmcnt(0)
	v_cvt_pk_bf16_f32 v7, v7, v8
	global_store_dword v[4:5], v7, off offset:128 nt
.LBB0_1184:
	s_or_b64 exec, exec, s[2:3]
	v_mul_f32_e32 v0, v23, v0
	ds_bpermute_b32 v7, v6, v0
	s_and_saveexec_b64 s[2:3], vcc
	s_cbranch_execz .LBB0_1186
	s_waitcnt lgkmcnt(0)
	v_cvt_pk_bf16_f32 v0, v0, v7
	global_store_dword v[4:5], v0, off offset:192 nt
.LBB0_1186:
	s_or_b64 exec, exec, s[2:3]
	ds_read_b32 v0, v161 offset:64
	v_lshlrev_b64 v[4:5], 12, v[144:145]
	v_lshl_add_u64 v[4:5], v[2:3], 0, v[4:5]
	s_mov_b64 s[2:3], 0x10000
	v_lshl_add_u64 v[4:5], v[4:5], 0, s[2:3]
	s_waitcnt lgkmcnt(0)
	v_rcp_f32_e32 v0, v0
	s_nop 0
	v_mul_f32_e32 v7, v72, v0
	ds_bpermute_b32 v8, v6, v7
	s_and_saveexec_b64 s[2:3], vcc
	s_cbranch_execz .LBB0_1188
	s_waitcnt lgkmcnt(0)
	v_cvt_pk_bf16_f32 v7, v7, v8
	global_store_dword v[4:5], v7, off nt
.LBB0_1188:
	s_or_b64 exec, exec, s[2:3]
	v_mul_f32_e32 v7, v56, v0
	s_waitcnt lgkmcnt(0)
	ds_bpermute_b32 v8, v6, v7
	s_and_saveexec_b64 s[2:3], vcc
	s_cbranch_execz .LBB0_1190
	s_waitcnt lgkmcnt(0)
	v_cvt_pk_bf16_f32 v7, v7, v8
	global_store_dword v[4:5], v7, off offset:64 nt
.LBB0_1190:
	s_or_b64 exec, exec, s[2:3]
	v_mul_f32_e32 v7, v40, v0
	s_waitcnt lgkmcnt(0)
	ds_bpermute_b32 v8, v6, v7
	s_and_saveexec_b64 s[2:3], vcc
	s_cbranch_execz .LBB0_1192
	s_waitcnt lgkmcnt(0)
	v_cvt_pk_bf16_f32 v7, v7, v8
	global_store_dword v[4:5], v7, off offset:128 nt
.LBB0_1192:
	s_or_b64 exec, exec, s[2:3]
	v_mul_f32_e32 v0, v24, v0
	ds_bpermute_b32 v7, v6, v0
	s_and_saveexec_b64 s[2:3], vcc
	s_cbranch_execz .LBB0_1194
	s_waitcnt lgkmcnt(0)
	v_cvt_pk_bf16_f32 v0, v0, v7
	global_store_dword v[4:5], v0, off offset:192 nt
.LBB0_1194:
	s_or_b64 exec, exec, s[2:3]
	ds_read_b32 v0, v161 offset:68
	v_lshlrev_b64 v[4:5], 12, v[144:145]
	v_lshl_add_u64 v[4:5], v[2:3], 0, v[4:5]
	s_mov_b64 s[2:3], 0x11000
	v_lshl_add_u64 v[4:5], v[4:5], 0, s[2:3]
	s_waitcnt lgkmcnt(0)
	v_rcp_f32_e32 v0, v0
	s_nop 0
	v_mul_f32_e32 v7, v73, v0
	ds_bpermute_b32 v8, v6, v7
	s_and_saveexec_b64 s[2:3], vcc
	s_cbranch_execz .LBB0_1196
	s_waitcnt lgkmcnt(0)
	v_cvt_pk_bf16_f32 v7, v7, v8
	global_store_dword v[4:5], v7, off nt
.LBB0_1196:
	s_or_b64 exec, exec, s[2:3]
	v_mul_f32_e32 v7, v57, v0
	s_waitcnt lgkmcnt(0)
	ds_bpermute_b32 v8, v6, v7
	s_and_saveexec_b64 s[2:3], vcc
	s_cbranch_execz .LBB0_1198
	s_waitcnt lgkmcnt(0)
	v_cvt_pk_bf16_f32 v7, v7, v8
	global_store_dword v[4:5], v7, off offset:64 nt
.LBB0_1198:
	s_or_b64 exec, exec, s[2:3]
	v_mul_f32_e32 v7, v41, v0
	s_waitcnt lgkmcnt(0)
	ds_bpermute_b32 v8, v6, v7
	s_and_saveexec_b64 s[2:3], vcc
	s_cbranch_execz .LBB0_1200
	s_waitcnt lgkmcnt(0)
	v_cvt_pk_bf16_f32 v7, v7, v8
	global_store_dword v[4:5], v7, off offset:128 nt
.LBB0_1200:
	s_or_b64 exec, exec, s[2:3]
	v_mul_f32_e32 v0, v25, v0
	ds_bpermute_b32 v7, v6, v0
	s_and_saveexec_b64 s[2:3], vcc
	s_cbranch_execz .LBB0_1202
	s_waitcnt lgkmcnt(0)
	v_cvt_pk_bf16_f32 v0, v0, v7
	global_store_dword v[4:5], v0, off offset:192 nt
.LBB0_1202:
	s_or_b64 exec, exec, s[2:3]
	ds_read_b32 v0, v161 offset:72
	v_lshlrev_b64 v[4:5], 12, v[144:145]
	v_lshl_add_u64 v[4:5], v[2:3], 0, v[4:5]
	s_mov_b64 s[2:3], 0x12000
	v_lshl_add_u64 v[4:5], v[4:5], 0, s[2:3]
	s_waitcnt lgkmcnt(0)
	v_rcp_f32_e32 v0, v0
	s_nop 0
	v_mul_f32_e32 v7, v74, v0
	ds_bpermute_b32 v8, v6, v7
	s_and_saveexec_b64 s[2:3], vcc
	s_cbranch_execz .LBB0_1204
	s_waitcnt lgkmcnt(0)
	v_cvt_pk_bf16_f32 v7, v7, v8
	global_store_dword v[4:5], v7, off nt
.LBB0_1204:
	s_or_b64 exec, exec, s[2:3]
	v_mul_f32_e32 v7, v58, v0
	s_waitcnt lgkmcnt(0)
	ds_bpermute_b32 v8, v6, v7
	s_and_saveexec_b64 s[2:3], vcc
	s_cbranch_execz .LBB0_1206
	s_waitcnt lgkmcnt(0)
	v_cvt_pk_bf16_f32 v7, v7, v8
	global_store_dword v[4:5], v7, off offset:64 nt
.LBB0_1206:
	s_or_b64 exec, exec, s[2:3]
	v_mul_f32_e32 v7, v42, v0
	s_waitcnt lgkmcnt(0)
	ds_bpermute_b32 v8, v6, v7
	s_and_saveexec_b64 s[2:3], vcc
	s_cbranch_execz .LBB0_1208
	s_waitcnt lgkmcnt(0)
	v_cvt_pk_bf16_f32 v7, v7, v8
	global_store_dword v[4:5], v7, off offset:128 nt
.LBB0_1208:
	s_or_b64 exec, exec, s[2:3]
	v_mul_f32_e32 v0, v26, v0
	ds_bpermute_b32 v7, v6, v0
	s_and_saveexec_b64 s[2:3], vcc
	s_cbranch_execz .LBB0_1210
	s_waitcnt lgkmcnt(0)
	v_cvt_pk_bf16_f32 v0, v0, v7
	global_store_dword v[4:5], v0, off offset:192 nt
.LBB0_1210:
	s_or_b64 exec, exec, s[2:3]
	ds_read_b32 v0, v161 offset:76
	v_lshlrev_b64 v[4:5], 12, v[144:145]
	v_lshl_add_u64 v[4:5], v[2:3], 0, v[4:5]
	s_mov_b64 s[2:3], 0x13000
	v_lshl_add_u64 v[4:5], v[4:5], 0, s[2:3]
	s_waitcnt lgkmcnt(0)
	v_rcp_f32_e32 v0, v0
	s_nop 0
	v_mul_f32_e32 v7, v75, v0
	ds_bpermute_b32 v8, v6, v7
	s_and_saveexec_b64 s[2:3], vcc
	s_cbranch_execz .LBB0_1212
	s_waitcnt lgkmcnt(0)
	v_cvt_pk_bf16_f32 v7, v7, v8
	global_store_dword v[4:5], v7, off nt
.LBB0_1212:
	s_or_b64 exec, exec, s[2:3]
	v_mul_f32_e32 v7, v59, v0
	s_waitcnt lgkmcnt(0)
	ds_bpermute_b32 v8, v6, v7
	s_and_saveexec_b64 s[2:3], vcc
	s_cbranch_execz .LBB0_1214
	s_waitcnt lgkmcnt(0)
	v_cvt_pk_bf16_f32 v7, v7, v8
	global_store_dword v[4:5], v7, off offset:64 nt
.LBB0_1214:
	s_or_b64 exec, exec, s[2:3]
	v_mul_f32_e32 v7, v43, v0
	s_waitcnt lgkmcnt(0)
	ds_bpermute_b32 v8, v6, v7
	s_and_saveexec_b64 s[2:3], vcc
	s_cbranch_execz .LBB0_1216
	s_waitcnt lgkmcnt(0)
	v_cvt_pk_bf16_f32 v7, v7, v8
	global_store_dword v[4:5], v7, off offset:128 nt
.LBB0_1216:
	s_or_b64 exec, exec, s[2:3]
	v_mul_f32_e32 v0, v27, v0
	ds_bpermute_b32 v7, v6, v0
	s_and_saveexec_b64 s[2:3], vcc
	s_cbranch_execz .LBB0_1218
	s_waitcnt lgkmcnt(0)
	v_cvt_pk_bf16_f32 v0, v0, v7
	global_store_dword v[4:5], v0, off offset:192 nt
.LBB0_1218:
	s_or_b64 exec, exec, s[2:3]
	ds_read_b32 v0, v161 offset:96
	v_lshlrev_b64 v[4:5], 12, v[144:145]
	v_lshl_add_u64 v[4:5], v[2:3], 0, v[4:5]
	s_mov_b64 s[2:3], 0x18000
	v_lshl_add_u64 v[4:5], v[4:5], 0, s[2:3]
	s_waitcnt lgkmcnt(0)
	v_rcp_f32_e32 v0, v0
	s_nop 0
	v_mul_f32_e32 v7, v76, v0
	ds_bpermute_b32 v8, v6, v7
	s_and_saveexec_b64 s[2:3], vcc
	s_cbranch_execz .LBB0_1220
	s_waitcnt lgkmcnt(0)
	v_cvt_pk_bf16_f32 v7, v7, v8
	global_store_dword v[4:5], v7, off nt
.LBB0_1220:
	s_or_b64 exec, exec, s[2:3]
	v_mul_f32_e32 v7, v60, v0
	s_waitcnt lgkmcnt(0)
	ds_bpermute_b32 v8, v6, v7
	s_and_saveexec_b64 s[2:3], vcc
	s_cbranch_execz .LBB0_1222
	s_waitcnt lgkmcnt(0)
	v_cvt_pk_bf16_f32 v7, v7, v8
	global_store_dword v[4:5], v7, off offset:64 nt
.LBB0_1222:
	s_or_b64 exec, exec, s[2:3]
	v_mul_f32_e32 v7, v44, v0
	s_waitcnt lgkmcnt(0)
	ds_bpermute_b32 v8, v6, v7
	s_and_saveexec_b64 s[2:3], vcc
	s_cbranch_execz .LBB0_1224
	s_waitcnt lgkmcnt(0)
	v_cvt_pk_bf16_f32 v7, v7, v8
	global_store_dword v[4:5], v7, off offset:128 nt
.LBB0_1224:
	s_or_b64 exec, exec, s[2:3]
	v_mul_f32_e32 v0, v28, v0
	ds_bpermute_b32 v7, v6, v0
	s_and_saveexec_b64 s[2:3], vcc
	s_cbranch_execz .LBB0_1226
	s_waitcnt lgkmcnt(0)
	v_cvt_pk_bf16_f32 v0, v0, v7
	global_store_dword v[4:5], v0, off offset:192 nt
.LBB0_1226:
	s_or_b64 exec, exec, s[2:3]
	ds_read_b32 v0, v161 offset:100
	v_lshlrev_b64 v[4:5], 12, v[144:145]
	v_lshl_add_u64 v[4:5], v[2:3], 0, v[4:5]
	s_mov_b64 s[2:3], 0x19000
	v_lshl_add_u64 v[4:5], v[4:5], 0, s[2:3]
	s_waitcnt lgkmcnt(0)
	v_rcp_f32_e32 v0, v0
	s_nop 0
	v_mul_f32_e32 v7, v77, v0
	ds_bpermute_b32 v8, v6, v7
	s_and_saveexec_b64 s[2:3], vcc
	s_cbranch_execz .LBB0_1228
	s_waitcnt lgkmcnt(0)
	v_cvt_pk_bf16_f32 v7, v7, v8
	global_store_dword v[4:5], v7, off nt
.LBB0_1228:
	s_or_b64 exec, exec, s[2:3]
	v_mul_f32_e32 v7, v61, v0
	s_waitcnt lgkmcnt(0)
	ds_bpermute_b32 v8, v6, v7
	s_and_saveexec_b64 s[2:3], vcc
	s_cbranch_execz .LBB0_1230
	s_waitcnt lgkmcnt(0)
	v_cvt_pk_bf16_f32 v7, v7, v8
	global_store_dword v[4:5], v7, off offset:64 nt
.LBB0_1230:
	s_or_b64 exec, exec, s[2:3]
	v_mul_f32_e32 v7, v45, v0
	s_waitcnt lgkmcnt(0)
	ds_bpermute_b32 v8, v6, v7
	s_and_saveexec_b64 s[2:3], vcc
	s_cbranch_execz .LBB0_1232
	s_waitcnt lgkmcnt(0)
	v_cvt_pk_bf16_f32 v7, v7, v8
	global_store_dword v[4:5], v7, off offset:128 nt
.LBB0_1232:
	s_or_b64 exec, exec, s[2:3]
	v_mul_f32_e32 v0, v29, v0
	ds_bpermute_b32 v7, v6, v0
	s_and_saveexec_b64 s[2:3], vcc
	s_cbranch_execz .LBB0_1234
	s_waitcnt lgkmcnt(0)
	v_cvt_pk_bf16_f32 v0, v0, v7
	global_store_dword v[4:5], v0, off offset:192 nt
.LBB0_1234:
	s_or_b64 exec, exec, s[2:3]
	ds_read_b32 v0, v161 offset:104
	v_lshlrev_b64 v[4:5], 12, v[144:145]
	v_lshl_add_u64 v[4:5], v[2:3], 0, v[4:5]
	s_mov_b64 s[2:3], 0x1a000
	v_lshl_add_u64 v[4:5], v[4:5], 0, s[2:3]
	s_waitcnt lgkmcnt(0)
	v_rcp_f32_e32 v0, v0
	s_nop 0
	v_mul_f32_e32 v7, v78, v0
	ds_bpermute_b32 v8, v6, v7
	s_and_saveexec_b64 s[2:3], vcc
	s_cbranch_execz .LBB0_1236
	s_waitcnt lgkmcnt(0)
	v_cvt_pk_bf16_f32 v7, v7, v8
	global_store_dword v[4:5], v7, off nt
.LBB0_1236:
	s_or_b64 exec, exec, s[2:3]
	v_mul_f32_e32 v7, v62, v0
	s_waitcnt lgkmcnt(0)
	ds_bpermute_b32 v8, v6, v7
	s_and_saveexec_b64 s[2:3], vcc
	s_cbranch_execz .LBB0_1238
	s_waitcnt lgkmcnt(0)
	v_cvt_pk_bf16_f32 v7, v7, v8
	global_store_dword v[4:5], v7, off offset:64 nt
.LBB0_1238:
	s_or_b64 exec, exec, s[2:3]
	v_mul_f32_e32 v7, v46, v0
	s_waitcnt lgkmcnt(0)
	ds_bpermute_b32 v8, v6, v7
	s_and_saveexec_b64 s[2:3], vcc
	s_cbranch_execz .LBB0_1240
	s_waitcnt lgkmcnt(0)
	v_cvt_pk_bf16_f32 v7, v7, v8
	global_store_dword v[4:5], v7, off offset:128 nt
.LBB0_1240:
	s_or_b64 exec, exec, s[2:3]
	v_mul_f32_e32 v0, v30, v0
	ds_bpermute_b32 v7, v6, v0
	s_and_saveexec_b64 s[2:3], vcc
	s_cbranch_execz .LBB0_1242
	s_waitcnt lgkmcnt(0)
	v_cvt_pk_bf16_f32 v0, v0, v7
	global_store_dword v[4:5], v0, off offset:192 nt
.LBB0_1242:
	s_or_b64 exec, exec, s[2:3]
	ds_read_b32 v0, v161 offset:108
	s_waitcnt lgkmcnt(2)
	v_lshlrev_b64 v[8:9], 12, v[144:145]
	v_lshl_add_u64 v[2:3], v[2:3], 0, v[8:9]
	s_mov_b64 s[2:3], 0x1b000
	v_lshl_add_u64 v[2:3], v[2:3], 0, s[2:3]
	s_waitcnt lgkmcnt(0)
	v_rcp_f32_e32 v0, v0
	s_nop 0
	v_mul_f32_e32 v4, v79, v0
	ds_bpermute_b32 v5, v6, v4
	s_and_saveexec_b64 s[2:3], vcc
	s_cbranch_execz .LBB0_1244
	s_waitcnt lgkmcnt(0)
	v_cvt_pk_bf16_f32 v4, v4, v5
	global_store_dword v[2:3], v4, off nt
.LBB0_1244:
	s_or_b64 exec, exec, s[2:3]
	v_mul_f32_e32 v4, v63, v0
	s_waitcnt lgkmcnt(0)
	ds_bpermute_b32 v5, v6, v4
	s_and_saveexec_b64 s[2:3], vcc
	s_cbranch_execz .LBB0_1246
	s_waitcnt lgkmcnt(0)
	v_cvt_pk_bf16_f32 v4, v4, v5
	global_store_dword v[2:3], v4, off offset:64 nt
.LBB0_1246:
	s_or_b64 exec, exec, s[2:3]
	v_mul_f32_e32 v4, v47, v0
	s_waitcnt lgkmcnt(0)
	ds_bpermute_b32 v5, v6, v4
	s_and_saveexec_b64 s[2:3], vcc
	s_cbranch_execz .LBB0_1248
	s_waitcnt lgkmcnt(0)
	v_cvt_pk_bf16_f32 v4, v4, v5
	global_store_dword v[2:3], v4, off offset:128 nt
.LBB0_1248:
	s_or_b64 exec, exec, s[2:3]
	v_mul_f32_e32 v0, v31, v0
	ds_bpermute_b32 v4, v6, v0
	s_and_saveexec_b64 s[2:3], vcc
	s_cbranch_execz .LBB0_1085
	s_waitcnt lgkmcnt(0)
	v_cvt_pk_bf16_f32 v0, v0, v4
	global_store_dword v[2:3], v0, off offset:192 nt
	s_branch .LBB0_1085
.LBB0_1250:
	s_cmpk_lt_i32 s67, 0x1080
	s_mov_b32 s60, s78
	s_waitcnt vmcnt(0) lgkmcnt(0)
	s_barrier
	v_mbcnt_lo_u32_b32 v20, -1, 0
	v_mbcnt_hi_u32_b32 v20, -1, v20
	s_cbranch_scc0 .LBB0_1259
	s_cmp_gt_u32 s67, 63
	s_cbranch_scc1 .LBB0_1259
	v_readlane_b32 s7, v250, 43
	v_readlane_b32 s20, v250, 46
	v_readlane_b32 s21, v250, 47
	v_readlane_b32 s36, v250, 48
	v_readlane_b32 s37, v250, 49
	s_lshr_b32 s28, s67, 4
	s_and_b32 s29, s67, 15
	s_mul_i32 s30, s28, 0x1080
	s_lshl_b32 s29, s29, 8
	s_mul_i32 s33, s67, 0x4200
	s_add_u32 s42, s74, s33
	s_addc_u32 s43, s75, 0
	s_add_u32 s42, s42, 0x500000
	s_addc_u32 s43, s43, 0
	s_lshl_b32 s33, s7, 3
	s_add_i32 s33, s33, 0x1c0
	v_mov_b32_e32 v54, s33
	global_load_dwordx2 v[18:19], v54, s[42:43]
	v_lshrrev_b32_e32 v55, 2, v20
	v_lshlrev_b32_e32 v56, 2, v55
	global_load_dword v57, v56, s[42:43] offset:448
	s_add_i32 s31, s30, 0x70
	s_lshl_b32 s31, s31, 12
	s_add_i32 s31, s31, s29
	v_and_b32_e32 v58, 3, v20
	v_lshlrev_b32_e32 v58, 6, v58
	v_lshl_add_u32 v59, v55, 12, v58
	v_add_u32_e32 v59, s31, v59
	global_load_dwordx4 v[2:5], v59, s[24:25]
	global_load_dwordx4 v[6:9], v59, s[24:25] offset:16
	global_load_dwordx4 v[10:13], v59, s[24:25] offset:32
	global_load_dwordx4 v[14:17], v59, s[24:25] offset:48
	s_lshl_b32 s34, s7, 13
	s_add_i32 s34, s34, s31
	v_add_u32_e32 v60, s34, v58
	v_add_u32_e32 v61, 0x1000, v60
	global_load_dwordx4 v[22:25], v60, s[20:21]
	global_load_dwordx4 v[26:29], v60, s[20:21] offset:16
	global_load_dwordx4 v[30:33], v60, s[20:21] offset:32
	global_load_dwordx4 v[34:37], v60, s[20:21] offset:48
	global_load_dwordx4 v[38:41], v61, s[20:21]
	global_load_dwordx4 v[42:45], v61, s[20:21] offset:16
	global_load_dwordx4 v[46:49], v61, s[20:21] offset:32
	global_load_dwordx4 v[50:53], v61, s[20:21] offset:48
	v_lshlrev_b32_e32 v62, 2, v20
	v_add_u32_e32 v62, s31, v62
	global_load_dword v64, v62, s[26:27]
	v_add_u32_e32 v62, 0x1000, v62
	global_load_dword v65, v62, s[26:27]
	v_add_u32_e32 v62, 0x1000, v62
	global_load_dword v66, v62, s[26:27]
	v_add_u32_e32 v62, 0x1000, v62
	global_load_dword v67, v62, s[26:27]
	v_add_u32_e32 v62, 0x1000, v62
	global_load_dword v68, v62, s[26:27]
	v_add_u32_e32 v62, 0x1000, v62
	global_load_dword v69, v62, s[26:27]
	v_add_u32_e32 v62, 0x1000, v62
	global_load_dword v70, v62, s[26:27]
	v_add_u32_e32 v62, 0x1000, v62
	global_load_dword v71, v62, s[26:27]
	v_add_u32_e32 v62, 0x1000, v62
	global_load_dword v72, v62, s[26:27]
	v_add_u32_e32 v62, 0x1000, v62
	global_load_dword v73, v62, s[26:27]
	v_add_u32_e32 v62, 0x1000, v62
	global_load_dword v74, v62, s[26:27]
	v_add_u32_e32 v62, 0x1000, v62
	global_load_dword v75, v62, s[26:27]
	v_add_u32_e32 v62, 0x1000, v62
	global_load_dword v76, v62, s[26:27]
	v_add_u32_e32 v62, 0x1000, v62
	global_load_dword v77, v62, s[26:27]
	v_add_u32_e32 v62, 0x1000, v62
	global_load_dword v78, v62, s[26:27]
	v_add_u32_e32 v62, 0x1000, v62
	global_load_dword v79, v62, s[26:27]
	s_mul_i32 s35, s7, 6
	s_add_i32 s35, s35, s30
	s_add_i32 s35, s35, 64
	s_lshl_b32 s35, s35, 12
	s_add_i32 s35, s35, s29
	v_lshlrev_b32_e32 v63, 2, v20
	v_add_u32_e32 v63, s35, v63
	v_mov_b32_e32 v80, 0
	global_store_dword v63, v80, s[36:37] nt
	v_add_u32_e32 v63, 0x1000, v63
	global_store_dword v63, v80, s[36:37] nt
	v_add_u32_e32 v63, 0x1000, v63
	global_store_dword v63, v80, s[36:37] nt
	v_add_u32_e32 v63, 0x1000, v63
	global_store_dword v63, v80, s[36:37] nt
	v_add_u32_e32 v63, 0x1000, v63
	global_store_dword v63, v80, s[36:37] nt
	v_add_u32_e32 v63, 0x1000, v63
	global_store_dword v63, v80, s[36:37] nt
	s_waitcnt vmcnt(0)
	v_mov_b32_e32 v81, 0
	v_mov_b32_e32 v82, 0
	v_lshlrev_b32_e32 v83, 16, v2
	v_and_b32_e32 v84, 0xffff0000, v2
	v_lshlrev_b32_e32 v85, 16, v22
	v_and_b32_e32 v86, 0xffff0000, v22
	v_fmac_f32_e32 v81, v83, v85
	v_fmac_f32_e32 v81, v84, v86
	v_lshlrev_b32_e32 v85, 16, v38
	v_and_b32_e32 v86, 0xffff0000, v38
	v_fmac_f32_e32 v82, v83, v85
	v_fmac_f32_e32 v82, v84, v86
	v_lshlrev_b32_e32 v83, 16, v3
	v_and_b32_e32 v84, 0xffff0000, v3
	v_lshlrev_b32_e32 v85, 16, v23
	v_and_b32_e32 v86, 0xffff0000, v23
	v_fmac_f32_e32 v81, v83, v85
	v_fmac_f32_e32 v81, v84, v86
	v_lshlrev_b32_e32 v85, 16, v39
	v_and_b32_e32 v86, 0xffff0000, v39
	v_fmac_f32_e32 v82, v83, v85
	v_fmac_f32_e32 v82, v84, v86
	v_lshlrev_b32_e32 v83, 16, v4
	v_and_b32_e32 v84, 0xffff0000, v4
	v_lshlrev_b32_e32 v85, 16, v24
	v_and_b32_e32 v86, 0xffff0000, v24
	v_fmac_f32_e32 v81, v83, v85
	v_fmac_f32_e32 v81, v84, v86
	v_lshlrev_b32_e32 v85, 16, v40
	v_and_b32_e32 v86, 0xffff0000, v40
	v_fmac_f32_e32 v82, v83, v85
	v_fmac_f32_e32 v82, v84, v86
	v_lshlrev_b32_e32 v83, 16, v5
	v_and_b32_e32 v84, 0xffff0000, v5
	v_lshlrev_b32_e32 v85, 16, v25
	v_and_b32_e32 v86, 0xffff0000, v25
	v_fmac_f32_e32 v81, v83, v85
	v_fmac_f32_e32 v81, v84, v86
	v_lshlrev_b32_e32 v85, 16, v41
	v_and_b32_e32 v86, 0xffff0000, v41
	v_fmac_f32_e32 v82, v83, v85
	v_fmac_f32_e32 v82, v84, v86
	v_lshlrev_b32_e32 v83, 16, v6
	v_and_b32_e32 v84, 0xffff0000, v6
	v_lshlrev_b32_e32 v85, 16, v26
	v_and_b32_e32 v86, 0xffff0000, v26
	v_fmac_f32_e32 v81, v83, v85
	v_fmac_f32_e32 v81, v84, v86
	v_lshlrev_b32_e32 v85, 16, v42
	v_and_b32_e32 v86, 0xffff0000, v42
	v_fmac_f32_e32 v82, v83, v85
	v_fmac_f32_e32 v82, v84, v86
	v_lshlrev_b32_e32 v83, 16, v7
	v_and_b32_e32 v84, 0xffff0000, v7
	v_lshlrev_b32_e32 v85, 16, v27
	v_and_b32_e32 v86, 0xffff0000, v27
	v_fmac_f32_e32 v81, v83, v85
	v_fmac_f32_e32 v81, v84, v86
	v_lshlrev_b32_e32 v85, 16, v43
	v_and_b32_e32 v86, 0xffff0000, v43
	v_fmac_f32_e32 v82, v83, v85
	v_fmac_f32_e32 v82, v84, v86
	v_lshlrev_b32_e32 v83, 16, v8
	v_and_b32_e32 v84, 0xffff0000, v8
	v_lshlrev_b32_e32 v85, 16, v28
	v_and_b32_e32 v86, 0xffff0000, v28
	v_fmac_f32_e32 v81, v83, v85
	v_fmac_f32_e32 v81, v84, v86
	v_lshlrev_b32_e32 v85, 16, v44
	v_and_b32_e32 v86, 0xffff0000, v44
	v_fmac_f32_e32 v82, v83, v85
	v_fmac_f32_e32 v82, v84, v86
	v_lshlrev_b32_e32 v83, 16, v9
	v_and_b32_e32 v84, 0xffff0000, v9
	v_lshlrev_b32_e32 v85, 16, v29
	v_and_b32_e32 v86, 0xffff0000, v29
	v_fmac_f32_e32 v81, v83, v85
	v_fmac_f32_e32 v81, v84, v86
	v_lshlrev_b32_e32 v85, 16, v45
	v_and_b32_e32 v86, 0xffff0000, v45
	v_fmac_f32_e32 v82, v83, v85
	v_fmac_f32_e32 v82, v84, v86
	v_lshlrev_b32_e32 v83, 16, v10
	v_and_b32_e32 v84, 0xffff0000, v10
	v_lshlrev_b32_e32 v85, 16, v30
	v_and_b32_e32 v86, 0xffff0000, v30
	v_fmac_f32_e32 v81, v83, v85
	v_fmac_f32_e32 v81, v84, v86
	v_lshlrev_b32_e32 v85, 16, v46
	v_and_b32_e32 v86, 0xffff0000, v46
	v_fmac_f32_e32 v82, v83, v85
	v_fmac_f32_e32 v82, v84, v86
	v_lshlrev_b32_e32 v83, 16, v11
	v_and_b32_e32 v84, 0xffff0000, v11
	v_lshlrev_b32_e32 v85, 16, v31
	v_and_b32_e32 v86, 0xffff0000, v31
	v_fmac_f32_e32 v81, v83, v85
	v_fmac_f32_e32 v81, v84, v86
	v_lshlrev_b32_e32 v85, 16, v47
	v_and_b32_e32 v86, 0xffff0000, v47
	v_fmac_f32_e32 v82, v83, v85
	v_fmac_f32_e32 v82, v84, v86
	v_lshlrev_b32_e32 v83, 16, v12
	v_and_b32_e32 v84, 0xffff0000, v12
	v_lshlrev_b32_e32 v85, 16, v32
	v_and_b32_e32 v86, 0xffff0000, v32
	v_fmac_f32_e32 v81, v83, v85
	v_fmac_f32_e32 v81, v84, v86
	v_lshlrev_b32_e32 v85, 16, v48
	v_and_b32_e32 v86, 0xffff0000, v48
	v_fmac_f32_e32 v82, v83, v85
	v_fmac_f32_e32 v82, v84, v86
	v_lshlrev_b32_e32 v83, 16, v13
	v_and_b32_e32 v84, 0xffff0000, v13
	v_lshlrev_b32_e32 v85, 16, v33
	v_and_b32_e32 v86, 0xffff0000, v33
	v_fmac_f32_e32 v81, v83, v85
	v_fmac_f32_e32 v81, v84, v86
	v_lshlrev_b32_e32 v85, 16, v49
	v_and_b32_e32 v86, 0xffff0000, v49
	v_fmac_f32_e32 v82, v83, v85
	v_fmac_f32_e32 v82, v84, v86
	v_lshlrev_b32_e32 v83, 16, v14
	v_and_b32_e32 v84, 0xffff0000, v14
	v_lshlrev_b32_e32 v85, 16, v34
	v_and_b32_e32 v86, 0xffff0000, v34
	v_fmac_f32_e32 v81, v83, v85
	v_fmac_f32_e32 v81, v84, v86
	v_lshlrev_b32_e32 v85, 16, v50
	v_and_b32_e32 v86, 0xffff0000, v50
	v_fmac_f32_e32 v82, v83, v85
	v_fmac_f32_e32 v82, v84, v86
	v_lshlrev_b32_e32 v83, 16, v15
	v_and_b32_e32 v84, 0xffff0000, v15
	v_lshlrev_b32_e32 v85, 16, v35
	v_and_b32_e32 v86, 0xffff0000, v35
	v_fmac_f32_e32 v81, v83, v85
	v_fmac_f32_e32 v81, v84, v86
	v_lshlrev_b32_e32 v85, 16, v51
	v_and_b32_e32 v86, 0xffff0000, v51
	v_fmac_f32_e32 v82, v83, v85
	v_fmac_f32_e32 v82, v84, v86
	v_lshlrev_b32_e32 v83, 16, v16
	v_and_b32_e32 v84, 0xffff0000, v16
	v_lshlrev_b32_e32 v85, 16, v36
	v_and_b32_e32 v86, 0xffff0000, v36
	v_fmac_f32_e32 v81, v83, v85
	v_fmac_f32_e32 v81, v84, v86
	v_lshlrev_b32_e32 v85, 16, v52
	v_and_b32_e32 v86, 0xffff0000, v52
	v_fmac_f32_e32 v82, v83, v85
	v_fmac_f32_e32 v82, v84, v86
	v_lshlrev_b32_e32 v83, 16, v17
	v_and_b32_e32 v84, 0xffff0000, v17
	v_lshlrev_b32_e32 v85, 16, v37
	v_and_b32_e32 v86, 0xffff0000, v37
	v_fmac_f32_e32 v81, v83, v85
	v_fmac_f32_e32 v81, v84, v86
	v_lshlrev_b32_e32 v85, 16, v53
	v_and_b32_e32 v86, 0xffff0000, v53
	v_fmac_f32_e32 v82, v83, v85
	v_fmac_f32_e32 v82, v84, v86
	s_nop 1
	v_add_f32_dpp v81, v81, v81 quad_perm:[1,0,3,2] row_mask:0xf bank_mask:0xf
	s_nop 1
	v_add_f32_dpp v81, v81, v81 quad_perm:[2,3,0,1] row_mask:0xf bank_mask:0xf
	s_nop 1
	v_add_f32_dpp v82, v82, v82 quad_perm:[1,0,3,2] row_mask:0xf bank_mask:0xf
	s_nop 1
	v_add_f32_dpp v82, v82, v82 quad_perm:[2,3,0,1] row_mask:0xf bank_mask:0xf
	s_mov_b32 s38, 0x3db504f3
	s_mov_b32 s40, 0x3fb8aa3b
	s_lshl_b32 s39, s7, 1
	v_mov_b32_e32 v99, 0xff800000
	v_sub_f32_e32 v87, v18, v57
	v_fma_f32 v81, v81, s38, v87
	v_cmp_ge_u32_e32 vcc, s39, v55
	s_nop 1
	v_cndmask_b32_e32 v81, v99, v81, vcc
	v_mov_b32_e32 v88, v81
	s_nop 1
	v_max_f32_dpp v88, v88, v88 row_ror:4 row_mask:0xf bank_mask:0xf
	s_nop 1
	v_max_f32_dpp v88, v88, v88 row_ror:8 row_mask:0xf bank_mask:0xf
	s_nop 1
	v_readlane_b32 s46, v88, 0
	v_readlane_b32 s47, v88, 16
	v_readlane_b32 s48, v88, 32
	v_readlane_b32 s49, v88, 48
	v_mov_b32_e32 v89, s46
	v_max_f32_e32 v89, s47, v89
	v_max_f32_e32 v89, s48, v89
	v_max_f32_e32 v89, s49, v89
	v_sub_f32_e32 v81, v81, v89
	v_mul_f32_e32 v81, s40, v81
	v_exp_f32_e32 v81, v81
	s_nop 0
	v_mov_b32_e32 v90, v81
	s_nop 1
	v_add_f32_dpp v90, v90, v90 row_ror:4 row_mask:0xf bank_mask:0xf
	s_nop 1
	v_add_f32_dpp v90, v90, v90 row_ror:8 row_mask:0xf bank_mask:0xf
	s_nop 1
	v_readlane_b32 s46, v90, 0
	v_readlane_b32 s47, v90, 16
	v_readlane_b32 s48, v90, 32
	v_readlane_b32 s49, v90, 48
	v_mov_b32_e32 v91, s46
	v_add_f32_e32 v91, s47, v91
	v_add_f32_e32 v91, s48, v91
	v_add_f32_e32 v91, s49, v91
	v_readlane_b32 s4, v81, 0
	v_readlane_b32 s5, v81, 4
	v_readlane_b32 s6, v81, 8
	v_readlane_b32 s7, v81, 12
	v_readlane_b32 s8, v81, 16
	v_readlane_b32 s9, v81, 20
	v_readlane_b32 s10, v81, 24
	v_readlane_b32 s11, v81, 28
	v_readlane_b32 s12, v81, 32
	v_readlane_b32 s13, v81, 36
	v_readlane_b32 s14, v81, 40
	v_readlane_b32 s15, v81, 44
	v_readlane_b32 s16, v81, 48
	v_readlane_b32 s17, v81, 52
	v_readlane_b32 s18, v81, 56
	v_readlane_b32 s19, v81, 60
	v_mov_b32_e32 v92, 0
	v_mov_b32_e32 v93, 0
	v_lshlrev_b32_e32 v94, 16, v64
	v_and_b32_e32 v95, 0xffff0000, v64
	v_fmac_f32_e32 v92, s4, v94
	v_fmac_f32_e32 v93, s4, v95
	v_lshlrev_b32_e32 v94, 16, v65
	v_and_b32_e32 v95, 0xffff0000, v65
	v_fmac_f32_e32 v92, s5, v94
	v_fmac_f32_e32 v93, s5, v95
	v_lshlrev_b32_e32 v94, 16, v66
	v_and_b32_e32 v95, 0xffff0000, v66
	v_fmac_f32_e32 v92, s6, v94
	v_fmac_f32_e32 v93, s6, v95
	v_lshlrev_b32_e32 v94, 16, v67
	v_and_b32_e32 v95, 0xffff0000, v67
	v_fmac_f32_e32 v92, s7, v94
	v_fmac_f32_e32 v93, s7, v95
	v_lshlrev_b32_e32 v94, 16, v68
	v_and_b32_e32 v95, 0xffff0000, v68
	v_fmac_f32_e32 v92, s8, v94
	v_fmac_f32_e32 v93, s8, v95
	v_lshlrev_b32_e32 v94, 16, v69
	v_and_b32_e32 v95, 0xffff0000, v69
	v_fmac_f32_e32 v92, s9, v94
	v_fmac_f32_e32 v93, s9, v95
	v_lshlrev_b32_e32 v94, 16, v70
	v_and_b32_e32 v95, 0xffff0000, v70
	v_fmac_f32_e32 v92, s10, v94
	v_fmac_f32_e32 v93, s10, v95
	v_lshlrev_b32_e32 v94, 16, v71
	v_and_b32_e32 v95, 0xffff0000, v71
	v_fmac_f32_e32 v92, s11, v94
	v_fmac_f32_e32 v93, s11, v95
	v_lshlrev_b32_e32 v94, 16, v72
	v_and_b32_e32 v95, 0xffff0000, v72
	v_fmac_f32_e32 v92, s12, v94
	v_fmac_f32_e32 v93, s12, v95
	v_lshlrev_b32_e32 v94, 16, v73
	v_and_b32_e32 v95, 0xffff0000, v73
	v_fmac_f32_e32 v92, s13, v94
	v_fmac_f32_e32 v93, s13, v95
	v_lshlrev_b32_e32 v94, 16, v74
	v_and_b32_e32 v95, 0xffff0000, v74
	v_fmac_f32_e32 v92, s14, v94
	v_fmac_f32_e32 v93, s14, v95
	v_lshlrev_b32_e32 v94, 16, v75
	v_and_b32_e32 v95, 0xffff0000, v75
	v_fmac_f32_e32 v92, s15, v94
	v_fmac_f32_e32 v93, s15, v95
	v_lshlrev_b32_e32 v94, 16, v76
	v_and_b32_e32 v95, 0xffff0000, v76
	v_fmac_f32_e32 v92, s16, v94
	v_fmac_f32_e32 v93, s16, v95
	v_lshlrev_b32_e32 v94, 16, v77
	v_and_b32_e32 v95, 0xffff0000, v77
	v_fmac_f32_e32 v92, s17, v94
	v_fmac_f32_e32 v93, s17, v95
	v_lshlrev_b32_e32 v94, 16, v78
	v_and_b32_e32 v95, 0xffff0000, v78
	v_fmac_f32_e32 v92, s18, v94
	v_fmac_f32_e32 v93, s18, v95
	v_lshlrev_b32_e32 v94, 16, v79
	v_and_b32_e32 v95, 0xffff0000, v79
	v_fmac_f32_e32 v92, s19, v94
	v_fmac_f32_e32 v93, s19, v95
	v_div_scale_f32 v96, s[46:47], v91, v91, 1.0
	v_rcp_f32_e32 v97, v96
	v_div_scale_f32 v98, vcc, 1.0, v91, 1.0
	v_fma_f32 v100, -v96, v97, 1.0
	v_fmac_f32_e32 v97, v100, v97
	v_mul_f32_e32 v100, v98, v97
	v_fma_f32 v101, -v96, v100, v98
	v_fmac_f32_e32 v100, v101, v97
	v_fma_f32 v96, -v96, v100, v98
	s_nop 1
	v_div_fmas_f32 v96, v96, v97, v100
	v_div_fixup_f32 v96, v96, v91, 1.0
	v_cmp_lt_f32_e32 vcc, 0, v91
	s_nop 1
	v_cndmask_b32_e32 v96, 0, v96, vcc
	v_mul_f32_e32 v92, v92, v96
	v_mul_f32_e32 v93, v93, v96
	v_cvt_pk_bf16_f32 v92, v92, v93
	v_lshlrev_b32_e32 v102, 2, v20
	v_add_u32_e32 v102, s34, v102
	global_store_dword v102, v92, s[36:37] nt
	v_sub_f32_e32 v87, v19, v57
	v_fma_f32 v82, v82, s38, v87
	s_add_i32 s39, s39, 1
	v_cmp_ge_u32_e32 vcc, s39, v55
	s_nop 1
	v_cndmask_b32_e32 v82, v99, v82, vcc
	v_mov_b32_e32 v88, v82
	s_nop 1
	v_max_f32_dpp v88, v88, v88 row_ror:4 row_mask:0xf bank_mask:0xf
	s_nop 1
	v_max_f32_dpp v88, v88, v88 row_ror:8 row_mask:0xf bank_mask:0xf
	s_nop 1
	v_readlane_b32 s46, v88, 0
	v_readlane_b32 s47, v88, 16
	v_readlane_b32 s48, v88, 32
	v_readlane_b32 s49, v88, 48
	v_mov_b32_e32 v89, s46
	v_max_f32_e32 v89, s47, v89
	v_max_f32_e32 v89, s48, v89
	v_max_f32_e32 v89, s49, v89
	v_sub_f32_e32 v82, v82, v89
	v_mul_f32_e32 v82, s40, v82
	v_exp_f32_e32 v82, v82
	s_nop 0
	v_mov_b32_e32 v90, v82
	s_nop 1
	v_add_f32_dpp v90, v90, v90 row_ror:4 row_mask:0xf bank_mask:0xf
	s_nop 1
	v_add_f32_dpp v90, v90, v90 row_ror:8 row_mask:0xf bank_mask:0xf
	s_nop 1
	v_readlane_b32 s46, v90, 0
	v_readlane_b32 s47, v90, 16
	v_readlane_b32 s48, v90, 32
	v_readlane_b32 s49, v90, 48
	v_mov_b32_e32 v91, s46
	v_add_f32_e32 v91, s47, v91
	v_add_f32_e32 v91, s48, v91
	v_add_f32_e32 v91, s49, v91
	v_readlane_b32 s4, v82, 0
	v_readlane_b32 s5, v82, 4
	v_readlane_b32 s6, v82, 8
	v_readlane_b32 s7, v82, 12
	v_readlane_b32 s8, v82, 16
	v_readlane_b32 s9, v82, 20
	v_readlane_b32 s10, v82, 24
	v_readlane_b32 s11, v82, 28
	v_readlane_b32 s12, v82, 32
	v_readlane_b32 s13, v82, 36
	v_readlane_b32 s14, v82, 40
	v_readlane_b32 s15, v82, 44
	v_readlane_b32 s16, v82, 48
	v_readlane_b32 s17, v82, 52
	v_readlane_b32 s18, v82, 56
	v_readlane_b32 s19, v82, 60
	v_mov_b32_e32 v92, 0
	v_mov_b32_e32 v93, 0
	v_lshlrev_b32_e32 v94, 16, v64
	v_and_b32_e32 v95, 0xffff0000, v64
	v_fmac_f32_e32 v92, s4, v94
	v_fmac_f32_e32 v93, s4, v95
	v_lshlrev_b32_e32 v94, 16, v65
	v_and_b32_e32 v95, 0xffff0000, v65
	v_fmac_f32_e32 v92, s5, v94
	v_fmac_f32_e32 v93, s5, v95
	v_lshlrev_b32_e32 v94, 16, v66
	v_and_b32_e32 v95, 0xffff0000, v66
	v_fmac_f32_e32 v92, s6, v94
	v_fmac_f32_e32 v93, s6, v95
	v_lshlrev_b32_e32 v94, 16, v67
	v_and_b32_e32 v95, 0xffff0000, v67
	v_fmac_f32_e32 v92, s7, v94
	v_fmac_f32_e32 v93, s7, v95
	v_lshlrev_b32_e32 v94, 16, v68
	v_and_b32_e32 v95, 0xffff0000, v68
	v_fmac_f32_e32 v92, s8, v94
	v_fmac_f32_e32 v93, s8, v95
	v_lshlrev_b32_e32 v94, 16, v69
	v_and_b32_e32 v95, 0xffff0000, v69
	v_fmac_f32_e32 v92, s9, v94
	v_fmac_f32_e32 v93, s9, v95
	v_lshlrev_b32_e32 v94, 16, v70
	v_and_b32_e32 v95, 0xffff0000, v70
	v_fmac_f32_e32 v92, s10, v94
	v_fmac_f32_e32 v93, s10, v95
	v_lshlrev_b32_e32 v94, 16, v71
	v_and_b32_e32 v95, 0xffff0000, v71
	v_fmac_f32_e32 v92, s11, v94
	v_fmac_f32_e32 v93, s11, v95
	v_lshlrev_b32_e32 v94, 16, v72
	v_and_b32_e32 v95, 0xffff0000, v72
	v_fmac_f32_e32 v92, s12, v94
	v_fmac_f32_e32 v93, s12, v95
	v_lshlrev_b32_e32 v94, 16, v73
	v_and_b32_e32 v95, 0xffff0000, v73
	v_fmac_f32_e32 v92, s13, v94
	v_fmac_f32_e32 v93, s13, v95
	v_lshlrev_b32_e32 v94, 16, v74
	v_and_b32_e32 v95, 0xffff0000, v74
	v_fmac_f32_e32 v92, s14, v94
	v_fmac_f32_e32 v93, s14, v95
	v_lshlrev_b32_e32 v94, 16, v75
	v_and_b32_e32 v95, 0xffff0000, v75
	v_fmac_f32_e32 v92, s15, v94
	v_fmac_f32_e32 v93, s15, v95
	v_lshlrev_b32_e32 v94, 16, v76
	v_and_b32_e32 v95, 0xffff0000, v76
	v_fmac_f32_e32 v92, s16, v94
	v_fmac_f32_e32 v93, s16, v95
	v_lshlrev_b32_e32 v94, 16, v77
	v_and_b32_e32 v95, 0xffff0000, v77
	v_fmac_f32_e32 v92, s17, v94
	v_fmac_f32_e32 v93, s17, v95
	v_lshlrev_b32_e32 v94, 16, v78
	v_and_b32_e32 v95, 0xffff0000, v78
	v_fmac_f32_e32 v92, s18, v94
	v_fmac_f32_e32 v93, s18, v95
	v_lshlrev_b32_e32 v94, 16, v79
	v_and_b32_e32 v95, 0xffff0000, v79
	v_fmac_f32_e32 v92, s19, v94
	v_fmac_f32_e32 v93, s19, v95
	v_div_scale_f32 v96, s[46:47], v91, v91, 1.0
	v_rcp_f32_e32 v97, v96
	v_div_scale_f32 v98, vcc, 1.0, v91, 1.0
	v_fma_f32 v100, -v96, v97, 1.0
	v_fmac_f32_e32 v97, v100, v97
	v_mul_f32_e32 v100, v98, v97
	v_fma_f32 v101, -v96, v100, v98
	v_fmac_f32_e32 v100, v101, v97
	v_fma_f32 v96, -v96, v100, v98
	s_nop 1
	v_div_fmas_f32 v96, v96, v97, v100
	v_div_fixup_f32 v96, v96, v91, 1.0
	v_cmp_lt_f32_e32 vcc, 0, v91
	s_nop 1
	v_cndmask_b32_e32 v96, 0, v96, vcc
	v_mul_f32_e32 v92, v92, v96
	v_mul_f32_e32 v93, v93, v96
	v_cvt_pk_bf16_f32 v92, v92, v93
	v_lshlrev_b32_e32 v102, 2, v20
	s_add_i32 s34, s34, 0x1000
	v_add_u32_e32 v102, s34, v102
	global_store_dword v102, v92, s[36:37] nt
	s_branch .LBB0_1259
